# M1: the next unit's token-index loads are no longer waited for before the current unit's K-loop; their result is consumed at the K-loop's row-switch point (in-order vmcnt guarantees arrival)
# baseline (speedup 1.0000x reference)
; #define PG8_GOFF(dst, U) do { _Pragma("unroll") for (int _h = 0; _h < 2; ++_h) _Pragma("unroll") for (int _i = 0; _i < 2; ++_i) { int _R, _C; stage_rc(tid * 16 + _i * 8192, _R, _C); dst[_h][_i] = (unsigned)S.gather_row(U, _h * HALF + _R); } } while (0)
;     ...
;         const bool has_next = S.next(ui + 1, nxt);
;         const char* nA = has_next ? nxt.A : cA; const char* nB = has_next ? nxt.B : cB;
;         if constexpr (GATHER) { if (has_next) PG8_GOFF(gn, nxt); }
; #pragma unroll 1
;         for (int t = 0; t < nt; t += 2) {
;             const bool last = (t == nt - 2);
;             const int t1 = kmod ? (t + 1) % kmod : t + 1, t2 = kmod ? (t + 2) % kmod : t + 2;
;             const char* a1 = cA + (size_t)t1 * kstep;
;             const char* a2 = last ? nA : cA + (size_t)t2 * kstep; const char* b2 = last ? nB : cB + (size_t)t2 * kstep;
;     ...
; #pragma unroll
;         for (int a = 0; a < 2; ++a)
; #pragma unroll
;             for (int b = 0; b < 2; ++b)
; #pragma unroll
;                 for (int m = 0; m < 4; ++m)
; #pragma unroll
;                     for (int n = 0; n < 2; ++n) acc[a][b][m][n] = (f32x4){0.f, 0.f, 0.f, 0.f};
.LBB0_1205:
	v_cndmask_b32_e64 v0, 0, 1, s[26:27]
	v_cmp_ne_u32_e64 s[4:5], 1, v0
	s_andn2_b64 vcc, exec, s[26:27]
	s_cbranch_vccnz .LBB0_1215
	s_ashr_i32 s17, s16, 31
	s_lshl_b32 s1, s57, 8
	s_lshl_b64 s[22:23], s[16:17], 18
	s_add_u32 s22, s54, s22
	s_addc_u32 s23, s61, s23
	v_mov_b32_e32 v225, 0
	v_mov_b32_e32 v226, 0
	v_mov_b32_e32 v227, 0
	v_mov_b32_e32 v228, 0
	s_waitcnt vmcnt(0)
	v_add_u32_e32 v0, s1, v214
	v_cmp_gt_i32_e32 vcc, s13, v0
	s_and_saveexec_b64 s[28:29], vcc
	v_lshlrev_b32_e32 v0, 3, v0
	global_load_dword v226, v0, s[22:23]
	s_or_b64 exec, exec, s[28:29]
	v_add_u32_e32 v0, s1, v215
	v_cmp_gt_i32_e32 vcc, s13, v0
	s_and_saveexec_b64 s[28:29], vcc
	v_lshlrev_b32_e32 v0, 3, v0
	global_load_dword v225, v0, s[22:23]
	s_or_b64 exec, exec, s[28:29]
	s_bitset1_b32 s1, 7
	v_add_u32_e32 v0, s1, v214
	v_cmp_gt_i32_e32 vcc, s13, v0
	s_and_saveexec_b64 s[28:29], vcc
	v_lshlrev_b32_e32 v0, 3, v0
	global_load_dword v228, v0, s[22:23]
	s_or_b64 exec, exec, s[28:29]
	v_add_u32_e32 v0, s1, v215
	v_cmp_gt_i32_e32 vcc, s13, v0
	s_and_saveexec_b64 s[28:29], vcc
	v_lshlrev_b32_e32 v0, 3, v0
	global_load_dword v227, v0, s[22:23]
	s_or_b64 exec, exec, s[28:29]
.LBB0_1215:
	s_and_b64 s[22:23], s[26:27], exec
	s_cselect_b32 s17, s11, s11
	s_cselect_b32 s25, s10, s10
	s_cselect_b32 s48, s21, s9
	s_cselect_b32 s49, s20, s8
	s_ashr_i32 s3, s2, 31
	s_lshl_b64 s[30:31], s[2:3], 13
	s_lshl_b32 s2, s6, 7
	s_ashr_i32 s3, s2, 31
	s_cmp_lg_u32 s0, 2
	s_cselect_b64 s[28:29], -1, 0
	s_cmp_lg_u32 s0, 1
	s_cselect_b64 s[22:23], -1, 0
	s_add_u32 s6, s45, s30
	s_addc_u32 s7, s41, s31
	s_lshl_b64 s[0:1], s[2:3], 2
	s_add_u32 s30, s6, s0
	s_addc_u32 s31, s7, s1
	s_waitcnt lgkmcnt(0)
	v_mov_b32_e32 v2, v1
	v_mov_b32_e32 v3, v1
	s_add_u32 s0, s8, 0x100
	v_mov_b32_e32 v0, v1
	v_mov_b64_e32 v[68:69], v[2:3]
	v_mov_b64_e32 v[72:73], v[2:3]
	v_mov_b64_e32 v[84:85], v[2:3]
	v_mov_b64_e32 v[88:89], v[2:3]
	v_mov_b64_e32 v[100:101], v[2:3]
	v_mov_b64_e32 v[104:105], v[2:3]
	v_mov_b64_e32 v[116:117], v[2:3]
	v_mov_b64_e32 v[120:121], v[2:3]
	v_mov_b64_e32 v[76:77], v[2:3]
	v_mov_b64_e32 v[80:81], v[2:3]
	v_mov_b64_e32 v[92:93], v[2:3]
	v_mov_b64_e32 v[96:97], v[2:3]
	v_mov_b64_e32 v[108:109], v[2:3]
	v_mov_b64_e32 v[112:113], v[2:3]
	v_mov_b64_e32 v[124:125], v[2:3]
	v_mov_b64_e32 v[128:129], v[2:3]
	v_mov_b64_e32 v[132:133], v[2:3]
	v_mov_b64_e32 v[136:137], v[2:3]
	v_mov_b64_e32 v[148:149], v[2:3]
	v_mov_b64_e32 v[152:153], v[2:3]
	v_mov_b64_e32 v[164:165], v[2:3]
	v_mov_b64_e32 v[168:169], v[2:3]
	v_mov_b64_e32 v[180:181], v[2:3]
	v_mov_b64_e32 v[184:185], v[2:3]
	v_mov_b64_e32 v[140:141], v[2:3]
	v_mov_b64_e32 v[144:145], v[2:3]
	v_mov_b64_e32 v[156:157], v[2:3]
	v_mov_b64_e32 v[160:161], v[2:3]
	v_mov_b64_e32 v[172:173], v[2:3]
	v_mov_b64_e32 v[176:177], v[2:3]
	v_mov_b64_e32 v[188:189], v[2:3]
	v_mov_b64_e32 v[192:193], v[2:3]
	s_addc_u32 s1, s9, 0
	s_mov_b32 s3, -2
	s_mov_b64 s[34:35], 0
	v_mov_b64_e32 v[66:67], v[0:1]
	v_mov_b64_e32 v[70:71], v[0:1]
	v_mov_b64_e32 v[82:83], v[0:1]
	v_mov_b64_e32 v[86:87], v[0:1]
	v_mov_b64_e32 v[98:99], v[0:1]
	v_mov_b64_e32 v[102:103], v[0:1]
	v_mov_b64_e32 v[114:115], v[0:1]
	v_mov_b64_e32 v[118:119], v[0:1]
	v_mov_b64_e32 v[74:75], v[0:1]
	v_mov_b64_e32 v[78:79], v[0:1]
	v_mov_b64_e32 v[90:91], v[0:1]
	v_mov_b64_e32 v[94:95], v[0:1]
	v_mov_b64_e32 v[106:107], v[0:1]
	v_mov_b64_e32 v[110:111], v[0:1]
	v_mov_b64_e32 v[122:123], v[0:1]
	v_mov_b64_e32 v[126:127], v[0:1]
	v_mov_b64_e32 v[130:131], v[0:1]
	v_mov_b64_e32 v[134:135], v[0:1]
	v_mov_b64_e32 v[146:147], v[0:1]
	v_mov_b64_e32 v[150:151], v[0:1]
	v_mov_b64_e32 v[162:163], v[0:1]
	v_mov_b64_e32 v[166:167], v[0:1]
	v_mov_b64_e32 v[178:179], v[0:1]
	v_mov_b64_e32 v[182:183], v[0:1]
	v_mov_b64_e32 v[138:139], v[0:1]
	v_mov_b64_e32 v[142:143], v[0:1]
	v_mov_b64_e32 v[154:155], v[0:1]
	v_mov_b64_e32 v[158:159], v[0:1]
	v_mov_b64_e32 v[170:171], v[0:1]
	v_mov_b64_e32 v[174:175], v[0:1]
	v_mov_b64_e32 v[186:187], v[0:1]
	v_mov_b64_e32 v[190:191], v[0:1]
	s_branch .LBB0_1217

; #define PG8_STAGE_A(bufoff, gbase, h, GO) do { if constexpr (GATHER) { PG8_STAGE(bufoff, gbase, (GO)[h]); } else { PG8_STAGE_U(bufoff, (const char*)(gbase) + (h) * hstepA, voffA, qstepA); } } while (0)
; #define PG8_LDA(dst, b, h) do { _Pragma("unroll") for (int m = 0; m < 4; ++m) _Pragma("unroll") for (int k = 0; k < 2; ++k) dst[m][k] = *(const LAS bf16x8*)(lds + PG8_SA(b, h) + aoff + m * 2048 + k * 1024); } while (0)
; #define PG8_LDB(dst, b, h) do { _Pragma("unroll") for (int n = 0; n < 2; ++n) _Pragma("unroll") for (int k = 0; k < 2; ++k) dst[n][k] = *(const LAS bf16x8*)(lds + PG8_SB(b, h) + boff + n * 2048 + k * 1024); } while (0)
; #define PG8_SCHED __builtin_amdgcn_sched_barrier(0)
;     ...
;             PG8_LDB(B0, 0, 0); PG8_LDB(B1, 0, 1); PG8_SCHED; PG8_LDA(At, 0, 0); PG8_STAGE_A(PG8_SA(1, 1), a1, 1, gc);
;             if constexpr (GATHER) { if (last && has_next) {
; #pragma unroll
;                 for (int h = 0; h < 2; ++h)
; #pragma unroll
;                     for (int i = 0; i < 2; ++i) { int _R, _C; stage_rc(tid * 16 + i * 8192, _R, _C); gc[h][i] = gn[h][i] * (unsigned)(lda * 2) + (unsigned)(_C * 2); } } }
.LBB0_1220:
	v_add_u32_e32 v0, 0x10000, v223
	ds_read_b128 v[18:21], v0
	ds_read_b128 v[22:25], v0 offset:1024
	ds_read_b128 v[26:29], v0 offset:2048
	ds_read_b128 v[30:33], v0 offset:3072
	v_add_u32_e32 v0, 0x14000, v223
	ds_read_b128 v[2:5], v0
	ds_read_b128 v[6:9], v0 offset:1024
	ds_read_b128 v[10:13], v0 offset:2048
	ds_read_b128 v[14:17], v0 offset:3072
	s_cmpk_eq_i32 s34, 0x300
	s_cselect_b64 s[8:9], -1, 0
	s_add_u32 s6, s10, s34
	v_mov_b32_e32 v0, v221
	s_addc_u32 s7, s11, s35
	s_waitcnt lgkmcnt(0)
	ds_read_b128 v[58:61], v224
	ds_read_b128 v[62:65], v224 offset:1024
	ds_read_b128 v[50:53], v224 offset:2048
	ds_read_b128 v[54:57], v224 offset:3072
	ds_read_b128 v[42:45], v224 offset:4096
	ds_read_b128 v[46:49], v224 offset:5120
	ds_read_b128 v[34:37], v224 offset:6144
	ds_read_b128 v[38:41], v224 offset:7168
	s_add_i32 m0, s63, 0xc000
	v_lshl_add_u64 v[194:195], s[6:7], 0, v[0:1]
	v_lshl_add_u64 v[194:195], v[194:195], 0, s[84:85]
	v_mov_b32_e32 v0, v220
	global_load_lds_dwordx4 v[194:195], off
	s_add_i32 m0, s63, 0xe000
	v_lshl_add_u64 v[194:195], s[6:7], 0, v[0:1]
	v_lshl_add_u64 v[194:195], v[194:195], 0, s[84:85]
	global_load_lds_dwordx4 v[194:195], off
	s_and_b64 s[6:7], s[26:27], s[8:9]
	s_andn2_b64 vcc, exec, s[6:7]
	s_cbranch_vccnz .LBB0_1222
	s_waitcnt vmcnt(8)
	v_ashrrev_i32_e32 v226, 2, v226
	v_ashrrev_i32_e32 v225, 2, v225
	v_ashrrev_i32_e32 v228, 2, v228
	v_ashrrev_i32_e32 v227, 2, v227
	v_lshl_add_u32 v229, v226, 10, v216
	v_lshl_add_u32 v230, v225, 10, v219
	v_lshl_add_u32 v231, v228, 10, v216
	v_lshl_add_u32 v232, v227, 10, v219
	v_mov_b32_e32 v220, v232
	v_mov_b32_e32 v221, v231
	v_mov_b32_e32 v222, v230
	v_mov_b32_e32 v218, v229
